# P11: waves 4-7 start half an iteration later (stagger) so the two waves of a SIMD alternate load and store phases
# speedup vs baseline: 1.0022x; 1.0022x over previous
; DI int opaque_tid() { int t = threadIdx.x; asm volatile("" : "+v"(t)); return t; }
; DI void p11_final(Frame& F, ArgsP A) {
;     const int ftid = opaque_tid(), flane = ftid & 63;
;     const bf16_t* X1 = (const bf16_t*)(A->ws + WS_X1B); const bf16_t* YK = (const bf16_t*)(A->ws + WS_YK); const float* gf = A->in[17];
;     const int gw = F.vcu * NWAVES + F.wave, NGW = F.G * NWAVES, lane = flane;
;     for (int row = gw; row < T; row += 2 * NGW) {
;         float va[32], vb[32];
;         const int row2 = row + NGW; const bool has2 = row2 < T;
;         p11_load(X1, YK, row, lane, va);
;         if (has2) p11_load(X1, YK, row2, lane, vb);
;         p11_store(A->out, gf, row, lane, va);
;         if (has2) p11_store(A->out, gf, row2, lane, vb);
;     }
; }
.LBB0_1064:
	s_cmp_lt_i32 s60, 12
	s_cselect_b64 s[2:3], -1, 0
	s_cmp_gt_i32 s61, 11
	s_cselect_b64 s[4:5], -1, 0
	s_and_b64 s[2:3], s[2:3], s[4:5]
	s_andn2_b64 vcc, exec, s[2:3]
	s_cbranch_vccnz .LBB0_1072
	s_lshl_b32 s2, s58, 3
	s_add_i32 s2, s2, s59
	s_cmpk_gt_i32 s2, 0x3fff
	s_cbranch_scc1 .LBB0_1072
	v_lshlrev_b32_e32 v1, 3, v0
	s_waitcnt vmcnt(0)
	v_and_b32_e32 v2, 0x1f8, v1
	v_mbcnt_lo_u32_b32 v1, -1, 0
	v_mbcnt_hi_u32_b32 v1, -1, v1
	v_and_b32_e32 v3, 64, v1
	v_add_u32_e32 v3, 64, v3
	v_xor_b32_e32 v4, 1, v1
	v_cmp_lt_i32_e32 vcc, v4, v3
	s_load_dwordx4 s[4:7], s[0:1], 0x88
	s_load_dwordx2 s[10:11], s[0:1], 0x98
	v_cndmask_b32_e32 v4, v1, v4, vcc
	v_lshlrev_b32_e32 v96, 2, v4
	v_xor_b32_e32 v4, 2, v1
	v_cmp_lt_i32_e32 vcc, v4, v3
	v_mov_b32_e32 v5, 0
	v_or_b32_e32 v6, 0x400, v2
	v_cndmask_b32_e32 v4, v1, v4, vcc
	v_lshlrev_b32_e32 v97, 2, v4
	v_xor_b32_e32 v4, 4, v1
	v_cmp_lt_i32_e32 vcc, v4, v3
	v_or_b32_e32 v8, 0x600, v2
	s_lshl_b32 s1, s58, 4
	v_cndmask_b32_e32 v4, v1, v4, vcc
	v_lshlrev_b32_e32 v98, 2, v4
	v_xor_b32_e32 v4, 8, v1
	v_cmp_lt_i32_e32 vcc, v4, v3
	s_lshl_b32 s3, s59, 1
	s_add_i32 s1, s1, s3
	v_cndmask_b32_e32 v4, v1, v4, vcc
	v_lshlrev_b32_e32 v99, 2, v4
	v_xor_b32_e32 v4, 16, v1
	v_cmp_lt_i32_e32 vcc, v4, v3
	s_ashr_i32 s3, s2, 31
	s_lshl_b32 s16, s33, 3
	v_cndmask_b32_e32 v4, v1, v4, vcc
	v_lshlrev_b32_e32 v100, 2, v4
	v_xor_b32_e32 v4, 32, v1
	v_cmp_lt_i32_e32 vcc, v4, v3
	s_lshl_b32 s0, s33, 4
	s_lshl_b32 s17, s33, 5
	v_cndmask_b32_e32 v1, v1, v4, vcc
	v_lshlrev_b32_e32 v4, 2, v2
	s_waitcnt lgkmcnt(0)
	v_lshl_add_u64 v[48:49], s[4:5], 0, v[4:5]
	v_lshlrev_b32_e32 v4, 2, v6
	v_lshl_add_u64 v[50:51], s[4:5], 0, v[4:5]
	v_lshlrev_b32_e32 v4, 2, v8
	v_lshl_add_u64 v[52:53], s[4:5], 0, v[4:5]
	v_lshlrev_b32_e32 v4, 1, v2
	v_lshl_add_u64 v[10:11], s[10:11], 0, v[4:5]
	s_mov_b64 s[4:5], 0x2000000
	v_lshl_add_u64 v[54:55], v[10:11], 0, s[4:5]
	s_or_b32 s4, s1, 1
	s_lshl_b64 s[8:9], s[2:3], 13
	v_and_b32_e32 v3, 63, v0
	s_add_u32 s8, s6, s8
	v_lshlrev_b32_e32 v4, 5, v3
	s_addc_u32 s9, s7, s9
	v_lshlrev_b32_e32 v101, 2, v1
	v_lshl_add_u64 v[0:1], s[8:9], 0, v[4:5]
	s_mov_b64 s[8:9], 0x1810
	s_ashr_i32 s1, s0, 31
	v_lshl_add_u64 v[58:59], v[0:1], 0, s[8:9]
	s_lshl_b64 s[8:9], s[0:1], 13
	s_lshl_b64 s[14:15], s[2:3], 12
	s_add_u32 s10, s10, s14
	v_lshlrev_b32_e32 v4, 4, v3
	s_addc_u32 s11, s11, s15
	s_mov_b64 s[12:13], 0x12200000
	v_lshl_add_u64 v[0:1], s[10:11], 0, v[4:5]
	v_lshl_add_u64 v[56:57], v[10:11], 0, s[12:13]
	v_lshl_add_u64 v[60:61], v[0:1], 0, s[12:13]
	s_lshl_b64 s[10:11], s[0:1], 12
	v_mov_b32_e32 v102, 0x358637bd
	s_mov_b32 s1, 0x800000
	s_movk_i32 s3, 0xf000
	v_lshlrev_b32_e32 v103, 2, v2
	v_lshlrev_b32_e32 v104, 2, v6
	v_lshlrev_b32_e32 v105, 2, v8
	s_cmp_ge_u32 s59, 4
	s_cbranch_scc0 .Lp11_nostag
	s_sleep 127
	s_sleep 127
.Lp11_nostag:
	s_branch .LBB0_1068
